# LN1 row loop: row-invariant gamma/beta/scale/shift read from LDS once per tile into registers instead of 16 ds_read_b128 per row; bf16 RNE bit-trick replaced by v_cvt_pk_bf16_f32
# speedup vs baseline: 1.0004x; 1.0004x over previous
; #define LAS __attribute__((address_space(3)))
; __device__ __forceinline__ unsigned pk2(float lo, float hi) { return f2bf(lo) | (f2bf(hi) << 16); }
; __device__ __forceinline__ float clamp8(float v) { return __builtin_amdgcn_fmed3f(v, -440.f, 440.f); }
; __device__ __forceinline__ void ln1_row(const u32x4 ra, const u32x4 rb, const LAS float* cv  , bf16_t* __restrict__ hf, unsigned char* __restrict__ hf8, float* __restrict__ stats, int row, int lane) {
;     ...
;     u32x4 ob[2], o8;
; #pragma unroll
;     for (int j = 0; j < 4; ++j) { const int col = c0 + 4 * j;
;         const f32x4 gg = *(const LAS f32x4*)(cv + col), bv = *(const LAS f32x4*)(cv + 1024 + col), sc1 = *(const LAS f32x4*)(cv + 2048 + col), sh = *(const LAS f32x4*)(cv + 3072 + col);
;         const f32x4 h4 = (v[j] * rstd * gg + bv) * sc1 + sh;
;         const unsigned p0 = pk2(h4.x, h4.y), p1 = pk2(h4.z, h4.w);
;         if (j == 0) { ob[0].x = p0; ob[0].y = p1; } else if (j == 1) { ob[0].z = p0; ob[0].w = p1; } else if (j == 2) { ob[1].x = p0; ob[1].y = p1; } else { ob[1].z = p0; ob[1].w = p1; }
;         const f32x4 h8 = h4 * S_HF8;
;         int w0 = __builtin_amdgcn_cvt_pk_fp8_f32(clamp8(h8.x), clamp8(h8.y), 0, false); w0 = __builtin_amdgcn_cvt_pk_fp8_f32(clamp8(h8.z), clamp8(h8.w), w0, true);
;         if (j == 0) o8.x = (unsigned)w0; else if (j == 1) o8.y = (unsigned)w0; else if (j == 2) o8.z = (unsigned)w0; else o8.w = (unsigned)w0; }
;     *(u32x4*)(hf + (size_t)row * D + c0) = ob[0]; *(u32x4*)(hf + (size_t)row * D + c0 + 8) = ob[1];
;     *(u32x4*)(hf8 + (size_t)row * D + c0) = o8;
.LBB0_414:
	s_or_b64 exec, exec, s[4:5]
	s_lshl_b32 s96, s2, 8
	v_readlane_b32 s4, v252, 42
	s_add_i32 s4, s96, s4
	s_ashr_i32 s5, s4, 31
	s_lshl_b64 s[4:5], s[4:5], 11
	v_lshlrev_b32_e32 v16, 4, v0
	s_add_u32 s4, s50, s4
	v_ashrrev_i32_e32 v17, 31, v16
	s_addc_u32 s5, s51, s5
	v_lshlrev_b64 v[2:3], 1, v[16:17]
	v_lshl_add_u64 v[18:19], s[4:5], 0, v[2:3]
	s_waitcnt lgkmcnt(0)
	s_barrier
	v_lshlrev_b32_e32 v122, 2, v16
	ds_read_b128 v[124:127], v122
	ds_read_b128 v[128:131], v122 offset:16
	ds_read_b128 v[132:135], v122 offset:32
	ds_read_b128 v[136:139], v122 offset:48
	ds_read_b128 v[140:143], v122 offset:4096
	ds_read_b128 v[144:147], v122 offset:4112
	ds_read_b128 v[148:151], v122 offset:8192
	ds_read_b128 v[152:155], v122 offset:8208
	ds_read_b128 v[156:159], v122 offset:12288
	ds_read_b128 v[162:165], v122 offset:12304
	ds_read_b128 v[166:169], v122 offset:4128
	ds_read_b128 v[170:173], v122 offset:4144
	ds_read_b128 v[174:177], v122 offset:8224
	ds_read_b128 v[178:181], v122 offset:8240
	ds_read_b128 v[182:185], v122 offset:12320
	ds_read_b128 v[186:189], v122 offset:12336
	global_load_dwordx4 v[12:15], v[18:19], off offset:16
	global_load_dwordx4 v[8:11], v[18:19], off
	v_lshl_add_u64 v[20:21], s[48:49], 0, v[2:3]
	v_lshl_add_u64 v[22:23], s[58:59], 0, v[16:17]
	v_cmp_ne_u32_e64 s[10:11], 0, v0
	s_movk_i32 s8, 0x400
	s_mov_b32 s6, s1
	global_load_dwordx4 v[114:117], v[18:19], off offset:2064
	global_load_dwordx4 v[118:121], v[18:19], off offset:2048
	s_mov_b32 s99, 0
	s_waitcnt vmcnt(2) lgkmcnt(0)
	s_branch .LBB0_416
.LBB0_415:
	s_or_b64 exec, exec, s[4:5]
	v_mov_b32_e32 v110, v40
	v_mov_b32_e32 v111, v38
	v_mov_b32_e32 v113, v8
	v_mov_b32_e32 v38, v41
	v_pk_mul_f32 v[40:41], v[110:111], v[44:45] op_sel_hi:[1,0]
	v_pk_mul_f32 v[38:39], v[38:39], v[44:45] op_sel_hi:[1,0]
	v_pk_fma_f32 v[40:41], v[40:41], v[124:125], v[140:141]
	v_pk_fma_f32 v[38:39], v[38:39], v[126:127], v[142:143]
	v_pk_fma_f32 v[40:41], v[40:41], v[148:149], v[156:157]
	v_mov_b32_e32 v13, v42
	v_pk_fma_f32 v[42:43], v[38:39], v[150:151], v[158:159]
	v_pk_mul_f32 v[38:39], v[40:41], s[88:89] op_sel_hi:[1,0]
	v_mov_b32_e32 v112, v36
	v_med3_f32 v8, v38, s27, v204
	v_med3_f32 v15, v39, s27, v204
	v_mov_b32_e32 v36, v24
	v_cvt_pk_fp8_f32 v36, v8, v15
	v_pk_mul_f32 v[38:39], v[42:43], s[88:89] op_sel_hi:[1,0]
	v_pk_mul_f32 v[32:33], v[32:33], v[44:45] op_sel_hi:[1,0]
	v_med3_f32 v8, v38, s27, v204
	v_med3_f32 v15, v39, s27, v204
	v_pk_mul_f32 v[38:39], v[112:113], v[44:45] op_sel_hi:[1,0]
	v_cvt_pk_fp8_f32 v36, v8, v15 op_sel:[0,0,1]
	v_pk_fma_f32 v[38:39], v[38:39], v[128:129], v[144:145]
	v_mov_b32_e32 v8, v37
	v_pk_fma_f32 v[46:47], v[38:39], v[152:153], v[162:163]
	v_pk_mul_f32 v[8:9], v[8:9], v[44:45] op_sel_hi:[1,0]
	v_pk_mul_f32 v[38:39], v[46:47], s[88:89] op_sel_hi:[1,0]
	v_mov_b32_e32 v37, v24
	v_med3_f32 v15, v38, s27, v204
	v_med3_f32 v17, v39, s27, v204
	v_pk_fma_f32 v[8:9], v[8:9], v[130:131], v[146:147]
	v_cvt_pk_fp8_f32 v37, v15, v17
	v_pk_fma_f32 v[8:9], v[8:9], v[154:155], v[164:165]
	v_pk_fma_f32 v[32:33], v[32:33], v[132:133], v[166:167]
	v_pk_mul_f32 v[38:39], v[8:9], s[88:89] op_sel_hi:[1,0]
	v_pk_fma_f32 v[32:33], v[32:33], v[174:175], v[182:183]
	v_med3_f32 v15, v38, s27, v204
	v_med3_f32 v17, v39, s27, v204
	v_pk_mul_f32 v[38:39], v[32:33], s[88:89] op_sel_hi:[1,0]
	v_cvt_pk_fp8_f32 v37, v15, v17 op_sel:[0,0,1]
	v_pk_mul_f32 v[34:35], v[34:35], v[44:45] op_sel_hi:[1,0]
	v_med3_f32 v15, v38, s27, v204
	v_med3_f32 v17, v39, s27, v204
	v_mov_b32_e32 v38, v24
	v_pk_fma_f32 v[34:35], v[34:35], v[134:135], v[168:169]
	v_cvt_pk_fp8_f32 v38, v15, v17
	v_pk_fma_f32 v[34:35], v[34:35], v[176:177], v[184:185]
	v_pk_mul_f32 v[12:13], v[12:13], v[44:45] op_sel_hi:[1,0]
	v_pk_mul_f32 v[48:49], v[34:35], s[88:89] op_sel_hi:[1,0]
	v_pk_fma_f32 v[12:13], v[12:13], v[136:137], v[170:171]
	v_med3_f32 v15, v48, s27, v204
	v_med3_f32 v17, v49, s27, v204
	v_cvt_pk_fp8_f32 v38, v15, v17 op_sel:[0,0,1]
	v_mov_b32_e32 v15, v26
	v_pk_mul_f32 v[14:15], v[14:15], v[44:45] op_sel_hi:[1,0]
	v_mov_b32_e32 v39, v24
	v_pk_fma_f32 v[14:15], v[14:15], v[138:139], v[172:173]
	v_pk_fma_f32 v[26:27], v[14:15], v[180:181], v[188:189]
	v_pk_fma_f32 v[14:15], v[12:13], v[178:179], v[186:187]
	v_pk_mul_f32 v[12:13], v[14:15], s[88:89] op_sel_hi:[1,0]
	v_med3_f32 v12, v12, s27, v204
	v_med3_f32 v13, v13, s27, v204
	v_cvt_pk_fp8_f32 v39, v12, v13
	v_pk_mul_f32 v[12:13], v[26:27], s[88:89] op_sel_hi:[1,0]
	v_med3_f32 v12, v12, s27, v204
	v_med3_f32 v13, v13, s27, v204
	v_cvt_pk_fp8_f32 v39, v12, v13 op_sel:[0,0,1]
	v_cvt_pk_bf16_f32 v12, v32, v33
	v_cvt_pk_bf16_f32 v13, v34, v35
	v_cvt_pk_bf16_f32 v14, v14, v15
	v_cvt_pk_bf16_f32 v15, v26, v27
	v_cvt_pk_bf16_f32 v32, v40, v41
	v_cvt_pk_bf16_f32 v33, v42, v43
	v_cvt_pk_bf16_f32 v34, v46, v47
	v_cvt_pk_bf16_f32 v35, v8, v9
	v_lshlrev_b64 v[8:9], 10, v[10:11]
	v_lshlrev_b64 v[10:11], 11, v[10:11]
	v_lshl_add_u64 v[10:11], v[20:21], 0, v[10:11]
	v_lshl_add_u64 v[8:9], v[22:23], 0, v[8:9]
	global_store_dwordx4 v[10:11], v[32:35], off
	global_store_dwordx4 v[10:11], v[12:15], off offset:16
	global_store_dwordx4 v[8:9], v[36:39], off
	s_addk_i32 s8, 0x400
	s_add_i32 s6, s6, 1
	s_waitcnt vmcnt(6)
	s_xor_b32 s99, s99, 1
	s_cbranch_scc0 .Lln1_cpA
	v_mov_b64_e32 v[10:11], v[120:121]
	v_mov_b64_e32 v[14:15], v[116:117]
	v_mov_b64_e32 v[8:9], v[118:119]
	v_mov_b64_e32 v[12:13], v[114:115]
	s_branch .Lln1_cp_done
